# prologue x->bf16 copy unrolled x4 (eight 16-byte loads in flight per lane)
# baseline (speedup 1.0000x reference)
; __device__ __forceinline__ unsigned pk2(float lo, float hi) { return f2bf(lo) | (f2bf(hi) << 16); }
; __global__ void __launch_bounds__(NTHR, 2) mk(Params p) {
;     ...
;         for (int i = blockIdx.x * NTHR + F.tid; i < T * DM / 8; i += F.G * NTHR) { const f32x4 a = *(const f32x4*)(p.in[0] + (size_t)i * 8), b = *(const f32x4*)(p.in[0] + (size_t)i * 8 + 4);
;             u32x4 w; w.x = pk2(a[0], a[1]); w.y = pk2(a[2], a[3]); w.z = pk2(b[0], b[1]); w.w = pk2(b[2], b[3]); *(u32x4*)(XB + (size_t)i * 8) = w; }
.Lcvtx_unr:
	s_mul_i32 m0, s4, 3
	v_add_u32_e32 v1, m0, v6
	v_cmp_ge_i32_e32 vcc, s13, v1
	s_xor_b64 vcc, vcc, exec
	s_cbranch_scc1 .Lcvtx_rem
	global_load_dwordx4 v[8:11], v[2:3], off offset:-16
	global_load_dwordx4 v[12:15], v[2:3], off
	v_lshl_add_u64 v[22:23], v[2:3], 0, s[6:7]
	global_load_dwordx4 v[24:27], v[22:23], off offset:-16
	global_load_dwordx4 v[28:31], v[22:23], off
	v_lshl_add_u64 v[22:23], v[22:23], 0, s[6:7]
	global_load_dwordx4 v[32:35], v[22:23], off offset:-16
	global_load_dwordx4 v[36:39], v[22:23], off
	v_lshl_add_u64 v[22:23], v[22:23], 0, s[6:7]
	global_load_dwordx4 v[40:43], v[22:23], off offset:-16
	global_load_dwordx4 v[44:47], v[22:23], off
	v_lshl_add_u64 v[22:23], v[22:23], 0, s[6:7]
	v_mov_b64_e32 v[2:3], v[22:23]
	s_waitcnt vmcnt(6)
	v_bfe_u32 v1, v8, 16, 1
	v_bfe_u32 v16, v10, 16, 1
	v_bfe_u32 v18, v12, 16, 1
	v_bfe_u32 v20, v14, 16, 1
	v_bfe_u32 v7, v9, 16, 1
	v_bfe_u32 v17, v11, 16, 1
	v_bfe_u32 v19, v13, 16, 1
	v_bfe_u32 v21, v15, 16, 1
	v_add3_u32 v1, v8, v1, s5
	v_add3_u32 v8, v10, v16, s5
	v_add3_u32 v10, v12, v18, s5
	v_add3_u32 v12, v14, v20, s5
	v_add3_u32 v7, v9, v7, s5
	v_add3_u32 v9, v11, v17, s5
	v_add3_u32 v11, v13, v19, s5
	v_add3_u32 v13, v15, v21, s5
	v_lshrrev_b32_e32 v1, 16, v1
	v_lshrrev_b32_e32 v14, 16, v8
	v_lshrrev_b32_e32 v10, 16, v10
	v_lshrrev_b32_e32 v12, 16, v12
	v_and_or_b32 v8, v7, s12, v1
	v_and_or_b32 v9, v9, s12, v14
	v_and_or_b32 v10, v11, s12, v10
	v_and_or_b32 v11, v13, s12, v12
	global_store_dwordx4 v[4:5], v[8:11], off
	v_lshl_add_u64 v[4:5], v[4:5], 0, s[8:9]
	s_waitcnt vmcnt(4)
	v_bfe_u32 v1, v24, 16, 1
	v_bfe_u32 v16, v26, 16, 1
	v_bfe_u32 v18, v28, 16, 1
	v_bfe_u32 v20, v30, 16, 1
	v_bfe_u32 v7, v25, 16, 1
	v_bfe_u32 v17, v27, 16, 1
	v_bfe_u32 v19, v29, 16, 1
	v_bfe_u32 v21, v31, 16, 1
	v_add3_u32 v1, v24, v1, s5
	v_add3_u32 v24, v26, v16, s5
	v_add3_u32 v26, v28, v18, s5
	v_add3_u32 v28, v30, v20, s5
	v_add3_u32 v7, v25, v7, s5
	v_add3_u32 v25, v27, v17, s5
	v_add3_u32 v27, v29, v19, s5
	v_add3_u32 v29, v31, v21, s5
	v_lshrrev_b32_e32 v1, 16, v1
	v_lshrrev_b32_e32 v30, 16, v24
	v_lshrrev_b32_e32 v26, 16, v26
	v_lshrrev_b32_e32 v28, 16, v28
	v_and_or_b32 v24, v7, s12, v1
	v_and_or_b32 v25, v25, s12, v30
	v_and_or_b32 v26, v27, s12, v26
	v_and_or_b32 v27, v29, s12, v28
	global_store_dwordx4 v[4:5], v[24:27], off
	v_lshl_add_u64 v[4:5], v[4:5], 0, s[8:9]
	s_waitcnt vmcnt(2)
	v_bfe_u32 v1, v32, 16, 1
	v_bfe_u32 v16, v34, 16, 1
	v_bfe_u32 v18, v36, 16, 1
	v_bfe_u32 v20, v38, 16, 1
	v_bfe_u32 v7, v33, 16, 1
	v_bfe_u32 v17, v35, 16, 1
	v_bfe_u32 v19, v37, 16, 1
	v_bfe_u32 v21, v39, 16, 1
	v_add3_u32 v1, v32, v1, s5
	v_add3_u32 v32, v34, v16, s5
	v_add3_u32 v34, v36, v18, s5
	v_add3_u32 v36, v38, v20, s5
	v_add3_u32 v7, v33, v7, s5
	v_add3_u32 v33, v35, v17, s5
	v_add3_u32 v35, v37, v19, s5
	v_add3_u32 v37, v39, v21, s5
	v_lshrrev_b32_e32 v1, 16, v1
	v_lshrrev_b32_e32 v38, 16, v32
	v_lshrrev_b32_e32 v34, 16, v34
	v_lshrrev_b32_e32 v36, 16, v36
	v_and_or_b32 v32, v7, s12, v1
	v_and_or_b32 v33, v33, s12, v38
	v_and_or_b32 v34, v35, s12, v34
	v_and_or_b32 v35, v37, s12, v36
	global_store_dwordx4 v[4:5], v[32:35], off
	v_lshl_add_u64 v[4:5], v[4:5], 0, s[8:9]
	s_waitcnt vmcnt(0)
	v_bfe_u32 v1, v40, 16, 1
	v_bfe_u32 v16, v42, 16, 1
	v_bfe_u32 v18, v44, 16, 1
	v_bfe_u32 v20, v46, 16, 1
	v_bfe_u32 v7, v41, 16, 1
	v_bfe_u32 v17, v43, 16, 1
	v_bfe_u32 v19, v45, 16, 1
	v_bfe_u32 v21, v47, 16, 1
	v_add3_u32 v1, v40, v1, s5
	v_add3_u32 v40, v42, v16, s5
	v_add3_u32 v42, v44, v18, s5
	v_add3_u32 v44, v46, v20, s5
	v_add3_u32 v7, v41, v7, s5
	v_add3_u32 v41, v43, v17, s5
	v_add3_u32 v43, v45, v19, s5
	v_add3_u32 v45, v47, v21, s5
	v_lshrrev_b32_e32 v1, 16, v1
	v_lshrrev_b32_e32 v46, 16, v40
	v_lshrrev_b32_e32 v42, 16, v42
	v_lshrrev_b32_e32 v44, 16, v44
	v_and_or_b32 v40, v7, s12, v1
	v_and_or_b32 v41, v41, s12, v46
	v_and_or_b32 v42, v43, s12, v42
	v_and_or_b32 v43, v45, s12, v44
	global_store_dwordx4 v[4:5], v[40:43], off
	v_lshl_add_u64 v[4:5], v[4:5], 0, s[8:9]
	s_lshl_b32 m0, s4, 2
	v_add_u32_e32 v6, m0, v6
	s_branch .Lcvtx_unr
.Lcvtx_rem:
	v_cmp_ge_i32_e32 vcc, s13, v6
	s_and_b64 exec, exec, vcc
	s_cbranch_execz .LBB0_81
